# nt hint also on the layer-1 rowpass residual reads and the merge epilogue gate reads
# baseline (speedup 1.0000x reference)
.LBB0_141:
	s_add_i32 s7, s14, 2
	s_cmp_ge_i32 s14, s12
	s_cselect_b64 s[38:39], -1, 0
	s_cmp_lt_i32 s14, s12
	s_waitcnt vmcnt(0)
	v_mov_b32_e32 v112, v32
	s_cselect_b32 s26, s7, s14
	v_lshlrev_b64 v[36:37], 10, v[112:113]
	v_mov_b32_e32 v112, v33
	s_ashr_i32 s27, s26, 31
	v_lshlrev_b64 v[32:33], 10, v[112:113]
	v_mov_b32_e32 v112, v34
	s_lshl_b64 s[26:27], s[26:27], 4
	v_readlane_b32 s28, v252, 8
	v_lshl_add_u64 v[72:73], s[94:95], 0, v[68:69]
	s_mov_b32 s15, 0xed40000
	v_lshlrev_b64 v[38:39], 10, v[112:113]
	v_mov_b32_e32 v112, v35
	v_readlane_b32 s29, v252, 9
	s_add_u32 s26, s28, s26
	v_add_co_u32_e32 v86, vcc, s15, v72
	v_lshlrev_b64 v[34:35], 10, v[112:113]
	s_addc_u32 s27, s29, s27
	v_addc_co_u32_e32 v87, vcc, 0, v73, vcc
	v_lshl_add_u64 v[36:37], v[62:63], 0, v[36:37]
	v_lshl_add_u64 v[32:33], v[62:63], 0, v[32:33]
	v_lshl_add_u64 v[38:39], v[62:63], 0, v[38:39]
	v_lshl_add_u64 v[34:35], v[62:63], 0, v[34:35]
	v_mov_b32_e32 v112, v56
	global_load_dwordx4 v[8:11], v113, s[26:27] offset:16
	global_load_dwordx4 v[12:15], v113, s[26:27]
	global_load_dwordx4 v[52:55], v[86:87], off nt
	global_load_dwordx4 v[48:51], v[86:87], off offset:1024 nt
	global_load_dwordx2 v[118:119], v[36:37], off nt
	global_load_dwordx2 v[116:117], v[32:33], off nt
	global_load_dwordx2 v[106:107], v[32:33], off offset:512 nt
	global_load_dwordx2 v[108:109], v[36:37], off offset:512 nt
	global_load_dwordx2 v[114:115], v[38:39], off nt
	global_load_dwordx2 v[110:111], v[34:35], off nt
	global_load_dwordx2 v[102:103], v[34:35], off offset:512 nt
	global_load_dwordx2 v[104:105], v[38:39], off offset:512 nt
	s_nop 0
	global_load_dwordx4 v[36:39], v[86:87], off offset:2048 nt
	global_load_dwordx4 v[32:35], v[86:87], off offset:3072 nt
	v_lshlrev_b64 v[86:87], 10, v[112:113]
	v_mov_b32_e32 v112, v57
	v_lshlrev_b64 v[56:57], 10, v[112:113]
	v_mov_b32_e32 v112, v58
	v_lshl_add_u64 v[92:93], v[62:63], 0, v[86:87]
	v_lshlrev_b64 v[86:87], 10, v[112:113]
	v_mov_b32_e32 v112, v59
	v_lshlrev_b64 v[58:59], 10, v[112:113]
	v_lshl_add_u64 v[56:57], v[62:63], 0, v[56:57]
	v_lshl_add_u64 v[58:59], v[62:63], 0, v[58:59]
	v_lshl_add_u64 v[120:121], v[62:63], 0, v[86:87]
	global_load_dwordx2 v[100:101], v[92:93], off nt
	global_load_dwordx2 v[98:99], v[56:57], off nt
	global_load_dwordx2 v[86:87], v[56:57], off offset:512 nt
	s_nop 0
	global_load_dwordx2 v[92:93], v[92:93], off offset:512 nt
	s_nop 0
	global_load_dwordx2 v[96:97], v[120:121], off nt
	global_load_dwordx2 v[94:95], v[58:59], off nt
	global_load_dwordx2 v[56:57], v[58:59], off offset:512 nt
	s_nop 0
	global_load_dwordx2 v[58:59], v[120:121], off offset:512 nt
	s_mul_hi_i32 s15, s14, 0x78787879
	s_lshr_b32 s25, s15, 31
	s_ashr_i32 s15, s15, 11
	s_add_i32 s15, s15, s25
	s_mul_i32 s25, s15, 0xffffef00
	s_add_i32 s25, s14, s25
	s_cmpk_gt_i32 s25, 0xff
	s_cselect_b32 s15, s15, 16
	s_cmp_eq_u32 s15, s13
	s_cbranch_scc1 .LBB0_143
	s_mul_i32 s25, s15, 0x6000
	s_mul_hi_i32 s13, s15, 0x6000
	s_add_u32 s26, s60, s25
	s_addc_u32 s27, s63, s13
	v_lshl_add_u64 v[0:1], s[26:27], 0, v[70:71]
	s_mov_b64 s[26:27], 0x5000
	v_lshl_add_u64 v[16:17], v[0:1], 0, s[26:27]
	v_add_co_u32_e32 v0, vcc, 0x5000, v0
	s_mov_b32 s26, 0x3d800000
	s_nop 0
	v_addc_co_u32_e32 v1, vcc, 0, v1, vcc
	global_load_dwordx4 v[0:3], v[0:1], off
	s_nop 0
	global_load_dwordx4 v[4:7], v[16:17], off offset:16
	global_load_dwordx4 v[20:23], v[16:17], off offset:2064
	s_nop 0
	global_load_dwordx4 v[16:19], v[16:17], off offset:2048
	s_add_i32 s13, s15, 17
	s_add_i32 s25, s25, 0x66000
	s_mul_hi_i32 s13, s13, 0x6000
	global_load_dwordx4 v[40:43], v[64:65], off offset:16
	global_load_dwordx4 v[44:47], v[64:65], off
	s_waitcnt vmcnt(5)
	v_pk_mul_f32 v[2:3], v[2:3], s[26:27] op_sel_hi:[1,0]
	v_pk_mul_f32 v[0:1], v[0:1], s[26:27] op_sel_hi:[1,0]
	s_waitcnt vmcnt(4)
	v_pk_mul_f32 v[6:7], v[6:7], s[26:27] op_sel_hi:[1,0]
	v_pk_mul_f32 v[4:5], v[4:5], s[26:27] op_sel_hi:[1,0]
	s_waitcnt vmcnt(2)
	v_pk_mul_f32 v[18:19], v[18:19], s[26:27] op_sel_hi:[1,0]
	v_pk_mul_f32 v[16:17], v[16:17], s[26:27] op_sel_hi:[1,0]
	v_pk_mul_f32 v[22:23], v[22:23], s[26:27] op_sel_hi:[1,0]
	v_pk_mul_f32 v[20:21], v[20:21], s[26:27] op_sel_hi:[1,0]
	s_add_u32 s26, s60, s25
	s_addc_u32 s27, s63, s13
	v_lshl_add_u64 v[128:129], s[26:27], 0, v[70:71]
	s_movk_i32 s13, 0x1000
	v_add_co_u32_e32 v24, vcc, s13, v128
	v_lshl_add_u64 v[88:89], v[128:129], 0, s[84:85]
	s_nop 0
	v_addc_co_u32_e32 v25, vcc, 0, v129, vcc
	global_load_dwordx4 v[74:77], v[24:25], off
	global_load_dwordx4 v[78:81], v[88:89], off offset:16
	s_nop 0
	global_load_dwordx4 v[24:27], v[128:129], off offset:16
	global_load_dwordx4 v[28:31], v[128:129], off
	global_load_dwordx4 v[120:123], v[64:65], off offset:2048
	global_load_dwordx4 v[124:127], v[64:65], off offset:2064
	global_load_dwordx4 v[82:85], v[88:89], off offset:2064
	s_nop 0
	global_load_dwordx4 v[88:91], v[88:89], off offset:2048
	s_mov_b32 s13, s15
	s_waitcnt vmcnt(7)
	v_pk_add_f32 v[76:77], v[76:77], 1.0 op_sel_hi:[1,0]
	v_pk_add_f32 v[74:75], v[74:75], 1.0 op_sel_hi:[1,0]
	s_waitcnt vmcnt(6)
	v_pk_add_f32 v[80:81], v[80:81], 1.0 op_sel_hi:[1,0]
	v_pk_add_f32 v[130:131], v[78:79], 1.0 op_sel_hi:[1,0]
	v_pk_mul_f32 v[76:77], v[46:47], v[76:77]
	v_pk_mul_f32 v[78:79], v[42:43], v[80:81]
	v_pk_mul_f32 v[74:75], v[44:45], v[74:75]
	v_pk_mul_f32 v[80:81], v[40:41], v[130:131]
	global_load_dwordx4 v[40:43], v[128:129], off offset:2064
	global_load_dwordx4 v[44:47], v[128:129], off offset:2048
	s_waitcnt vmcnt(2)
	v_pk_add_f32 v[90:91], v[90:91], 1.0 op_sel_hi:[1,0]
	v_pk_add_f32 v[84:85], v[84:85], 1.0 op_sel_hi:[1,0]
	v_pk_add_f32 v[132:133], v[88:89], 1.0 op_sel_hi:[1,0]
	v_pk_add_f32 v[134:135], v[82:83], 1.0 op_sel_hi:[1,0]
	v_pk_mul_f32 v[88:89], v[126:127], v[84:85]
	v_pk_mul_f32 v[82:83], v[122:123], v[90:91]
	v_pk_mul_f32 v[90:91], v[124:125], v[134:135]
	v_pk_mul_f32 v[84:85], v[120:121], v[132:133]
